# ordered-emission pass: key ids of groups 1-3 formed with one 32-bit literal add instead of s_mov_b64 + 64-bit add (42 instructions fewer per 64 keys)
# speedup vs baseline: 1.0052x; 1.0045x over previous
.LBB0_845:
	s_or_b64 exec, exec, s[24:25]
	s_andn2_b64 vcc, exec, s[18:19]
	s_cbranch_vccnz .LBB0_975
	ds_read_u16 v2, v50 offset:36896
	s_waitcnt lgkmcnt(0)
	v_cmp_ne_u16_e32 vcc, 0, v2
	s_and_saveexec_b64 s[18:19], vcc
	s_cbranch_execz .LBB0_973
	ds_read_u16 v2, v49 offset:36896
	s_waitcnt vmcnt(7)
	v_add_u32_e32 v28, 0x11220, v49
	ds_read_b32 v28, v28
	v_lshl_add_u64 v[30:31], v[40:41], 0, s[16:17]
	s_waitcnt vmcnt(4)
	s_waitcnt lgkmcnt(1)
	v_lshrrev_b32_e32 v29, 8, v2
	v_and_b32_e32 v2, 0xff, v2
	v_cndmask_b32_e64 v29, v29, 0, s[22:23]
	v_cndmask_b32_e64 v2, v2, 0, s[22:23]
	s_waitcnt lgkmcnt(0)
	v_add_u32_sdwa v34, v29, v28 dst_sel:DWORD dst_unused:UNUSED_PAD src0_sel:DWORD src1_sel:WORD_1
	v_add_u32_sdwa v35, v2, v28 dst_sel:DWORD dst_unused:UNUSED_PAD src0_sel:DWORD src1_sel:WORD_0
	v_lshl_add_u64 v[28:29], v[30:31], 0, s[84:85]
	v_min_i32_e32 v2, v34, v37
	v_add_u32_e32 v2, v2, v35
	v_sub_u32_e32 v34, v37, v34
	v_med3_i32 v35, v34, 0, 1
	v_sub_u32_e32 v35, v36, v35
	v_cmp_gt_i32_sdwa s[0:1], v24, v35 src0_sel:WORD_0 src1_sel:DWORD
	v_cmp_eq_u32_sdwa s[24:25], v24, v36 src0_sel:WORD_0 src1_sel:DWORD
	v_lshl_add_u64 v[32:33], v[2:3], 1, v[38:39]
	s_and_saveexec_b64 s[30:31], s[0:1]
	global_store_short v[32:33], v28, off
	s_mov_b64 exec, s[30:31]
	v_addc_co_u32_e64 v2, vcc, 0, v2, s[0:1]
	v_subb_co_u32_e64 v34, vcc, v34, 0, s[24:25]
	v_add_u32_e32 v32, 0x101, v30
	v_med3_i32 v35, v34, 0, 1
	v_sub_u32_e32 v35, v36, v35
	v_cmp_gt_i32_sdwa s[0:1], v24, v35 src0_sel:WORD_1 src1_sel:DWORD
	v_cmp_eq_u32_sdwa s[24:25], v24, v36 src0_sel:WORD_1 src1_sel:DWORD
	v_lshl_add_u64 v[44:45], v[2:3], 1, v[38:39]
	s_and_saveexec_b64 s[30:31], s[0:1]
	global_store_short v[44:45], v32, off
	s_mov_b64 exec, s[30:31]
	v_addc_co_u32_e64 v2, vcc, 0, v2, s[0:1]
	v_subb_co_u32_e64 v34, vcc, v34, 0, s[24:25]
	v_add_u32_e32 v32, 0x102, v30
	v_med3_i32 v35, v34, 0, 1
	v_sub_u32_e32 v35, v36, v35
	v_cmp_gt_i32_sdwa s[0:1], v25, v35 src0_sel:WORD_0 src1_sel:DWORD
	v_cmp_eq_u32_sdwa s[24:25], v25, v36 src0_sel:WORD_0 src1_sel:DWORD
	v_lshl_add_u64 v[44:45], v[2:3], 1, v[38:39]
	s_and_saveexec_b64 s[30:31], s[0:1]
	global_store_short v[44:45], v32, off
	s_mov_b64 exec, s[30:31]
	v_addc_co_u32_e64 v2, vcc, 0, v2, s[0:1]
	v_subb_co_u32_e64 v34, vcc, v34, 0, s[24:25]
	v_add_u32_e32 v32, 0x103, v30
	v_med3_i32 v35, v34, 0, 1
	v_sub_u32_e32 v35, v36, v35
	v_cmp_gt_i32_sdwa s[0:1], v25, v35 src0_sel:WORD_1 src1_sel:DWORD
	v_cmp_eq_u32_sdwa s[24:25], v25, v36 src0_sel:WORD_1 src1_sel:DWORD
	v_lshl_add_u64 v[24:25], v[2:3], 1, v[38:39]
	s_and_saveexec_b64 s[30:31], s[0:1]
	global_store_short v[24:25], v32, off
	s_mov_b64 exec, s[30:31]
	v_addc_co_u32_e64 v2, vcc, 0, v2, s[0:1]
	v_subb_co_u32_e64 v34, vcc, v34, 0, s[24:25]
	v_add_u32_e32 v24, 0x104, v30
	v_med3_i32 v35, v34, 0, 1
	v_sub_u32_e32 v35, v36, v35
	v_cmp_gt_i32_sdwa s[0:1], v26, v35 src0_sel:WORD_0 src1_sel:DWORD
	v_cmp_eq_u32_sdwa s[24:25], v26, v36 src0_sel:WORD_0 src1_sel:DWORD
	v_lshl_add_u64 v[32:33], v[2:3], 1, v[38:39]
	s_and_saveexec_b64 s[30:31], s[0:1]
	global_store_short v[32:33], v24, off
	s_mov_b64 exec, s[30:31]
	v_addc_co_u32_e64 v2, vcc, 0, v2, s[0:1]
	v_subb_co_u32_e64 v34, vcc, v34, 0, s[24:25]
	v_add_u32_e32 v24, 0x105, v30
	v_med3_i32 v35, v34, 0, 1
	v_sub_u32_e32 v35, v36, v35
	v_cmp_gt_i32_sdwa s[0:1], v26, v35 src0_sel:WORD_1 src1_sel:DWORD
	v_cmp_eq_u32_sdwa s[24:25], v26, v36 src0_sel:WORD_1 src1_sel:DWORD
	v_lshl_add_u64 v[32:33], v[2:3], 1, v[38:39]
	s_and_saveexec_b64 s[30:31], s[0:1]
	global_store_short v[32:33], v24, off
	s_mov_b64 exec, s[30:31]
	v_addc_co_u32_e64 v2, vcc, 0, v2, s[0:1]
	v_subb_co_u32_e64 v34, vcc, v34, 0, s[24:25]
	v_add_u32_e32 v24, 0x106, v30
	v_med3_i32 v35, v34, 0, 1
	v_sub_u32_e32 v35, v36, v35
	v_cmp_gt_i32_sdwa s[0:1], v27, v35 src0_sel:WORD_0 src1_sel:DWORD
	v_cmp_eq_u32_sdwa s[24:25], v27, v36 src0_sel:WORD_0 src1_sel:DWORD
	v_lshl_add_u64 v[32:33], v[2:3], 1, v[38:39]
	s_and_saveexec_b64 s[30:31], s[0:1]
	global_store_short v[32:33], v24, off
	s_mov_b64 exec, s[30:31]
	v_addc_co_u32_e64 v2, vcc, 0, v2, s[0:1]
	v_subb_co_u32_e64 v34, vcc, v34, 0, s[24:25]
	v_add_u32_e32 v24, 0x107, v30
	v_med3_i32 v35, v34, 0, 1
	v_sub_u32_e32 v35, v36, v35
	v_cmp_gt_i32_sdwa s[0:1], v27, v35 src0_sel:WORD_1 src1_sel:DWORD
	v_cmp_eq_u32_sdwa s[24:25], v27, v36 src0_sel:WORD_1 src1_sel:DWORD
	v_lshl_add_u64 v[26:27], v[2:3], 1, v[38:39]
	s_and_saveexec_b64 s[30:31], s[0:1]
	global_store_short v[26:27], v24, off
	s_mov_b64 exec, s[30:31]
	v_addc_co_u32_e64 v2, vcc, 0, v2, s[0:1]
	v_subb_co_u32_e64 v34, vcc, v34, 0, s[24:25]
	v_add_u32_e32 v24, 0x108, v30
	v_med3_i32 v35, v34, 0, 1
	v_sub_u32_e32 v35, v36, v35
	v_cmp_gt_i32_sdwa s[0:1], v20, v35 src0_sel:WORD_0 src1_sel:DWORD
	v_cmp_eq_u32_sdwa s[24:25], v20, v36 src0_sel:WORD_0 src1_sel:DWORD
	v_lshl_add_u64 v[26:27], v[2:3], 1, v[38:39]
	s_and_saveexec_b64 s[30:31], s[0:1]
	global_store_short v[26:27], v24, off
	s_mov_b64 exec, s[30:31]
	v_addc_co_u32_e64 v2, vcc, 0, v2, s[0:1]
	v_subb_co_u32_e64 v34, vcc, v34, 0, s[24:25]
	v_add_u32_e32 v24, 0x109, v30
	v_med3_i32 v35, v34, 0, 1
	v_sub_u32_e32 v35, v36, v35
	v_cmp_gt_i32_sdwa s[0:1], v20, v35 src0_sel:WORD_1 src1_sel:DWORD
	v_cmp_eq_u32_sdwa s[24:25], v20, v36 src0_sel:WORD_1 src1_sel:DWORD
	v_lshl_add_u64 v[26:27], v[2:3], 1, v[38:39]
	s_and_saveexec_b64 s[30:31], s[0:1]
	global_store_short v[26:27], v24, off
	s_mov_b64 exec, s[30:31]
	v_addc_co_u32_e64 v2, vcc, 0, v2, s[0:1]
	v_subb_co_u32_e64 v34, vcc, v34, 0, s[24:25]
	v_add_u32_e32 v24, 0x10a, v30
	v_med3_i32 v35, v34, 0, 1
	v_sub_u32_e32 v35, v36, v35
	v_cmp_gt_i32_sdwa s[0:1], v21, v35 src0_sel:WORD_0 src1_sel:DWORD
	v_cmp_eq_u32_sdwa s[24:25], v21, v36 src0_sel:WORD_0 src1_sel:DWORD
	v_lshl_add_u64 v[26:27], v[2:3], 1, v[38:39]
	s_and_saveexec_b64 s[30:31], s[0:1]
	global_store_short v[26:27], v24, off
	s_mov_b64 exec, s[30:31]
	v_addc_co_u32_e64 v2, vcc, 0, v2, s[0:1]
	v_subb_co_u32_e64 v34, vcc, v34, 0, s[24:25]
	v_add_u32_e32 v24, 0x10b, v30
	v_med3_i32 v35, v34, 0, 1
	v_sub_u32_e32 v35, v36, v35
	v_cmp_gt_i32_sdwa s[0:1], v21, v35 src0_sel:WORD_1 src1_sel:DWORD
	v_cmp_eq_u32_sdwa s[24:25], v21, v36 src0_sel:WORD_1 src1_sel:DWORD
	v_lshl_add_u64 v[20:21], v[2:3], 1, v[38:39]
	s_and_saveexec_b64 s[30:31], s[0:1]
	global_store_short v[20:21], v24, off
	s_mov_b64 exec, s[30:31]
	v_addc_co_u32_e64 v2, vcc, 0, v2, s[0:1]
	v_subb_co_u32_e64 v34, vcc, v34, 0, s[24:25]
	v_add_u32_e32 v20, 0x10c, v30
	v_med3_i32 v35, v34, 0, 1
	v_sub_u32_e32 v35, v36, v35
	v_cmp_gt_i32_sdwa s[0:1], v22, v35 src0_sel:WORD_0 src1_sel:DWORD
	v_cmp_eq_u32_sdwa s[24:25], v22, v36 src0_sel:WORD_0 src1_sel:DWORD
	v_lshl_add_u64 v[24:25], v[2:3], 1, v[38:39]
	s_and_saveexec_b64 s[30:31], s[0:1]
	global_store_short v[24:25], v20, off
	s_mov_b64 exec, s[30:31]
	v_addc_co_u32_e64 v2, vcc, 0, v2, s[0:1]
	v_subb_co_u32_e64 v34, vcc, v34, 0, s[24:25]
	v_add_u32_e32 v20, 0x10d, v30
	v_med3_i32 v35, v34, 0, 1
	v_sub_u32_e32 v35, v36, v35
	v_cmp_gt_i32_sdwa s[0:1], v22, v35 src0_sel:WORD_1 src1_sel:DWORD
	v_cmp_eq_u32_sdwa s[24:25], v22, v36 src0_sel:WORD_1 src1_sel:DWORD
	v_lshl_add_u64 v[24:25], v[2:3], 1, v[38:39]
	s_and_saveexec_b64 s[30:31], s[0:1]
	global_store_short v[24:25], v20, off
	s_mov_b64 exec, s[30:31]
	v_addc_co_u32_e64 v2, vcc, 0, v2, s[0:1]
	v_subb_co_u32_e64 v34, vcc, v34, 0, s[24:25]
	v_add_u32_e32 v20, 0x10e, v30
	v_med3_i32 v35, v34, 0, 1
	v_sub_u32_e32 v35, v36, v35
	v_cmp_gt_i32_sdwa s[0:1], v23, v35 src0_sel:WORD_0 src1_sel:DWORD
	v_cmp_eq_u32_sdwa s[24:25], v23, v36 src0_sel:WORD_0 src1_sel:DWORD
	v_lshl_add_u64 v[24:25], v[2:3], 1, v[38:39]
	s_and_saveexec_b64 s[30:31], s[0:1]
	global_store_short v[24:25], v20, off
	s_mov_b64 exec, s[30:31]
	v_addc_co_u32_e64 v2, vcc, 0, v2, s[0:1]
	v_subb_co_u32_e64 v34, vcc, v34, 0, s[24:25]
	v_sub_u32_e32 v34, v37, v34
	v_min_i32_e32 v35, v34, v37
	v_sub_u32_e32 v35, v2, v35
	v_cmp_le_u32_sdwa s[24:25], v23, v36 src0_sel:WORD_1 src1_sel:DWORD
	s_mov_b64 s[0:1], 0
	s_and_saveexec_b64 s[30:31], s[24:25]
	s_xor_b64 s[24:25], exec, s[30:31]
	s_cbranch_execz .LBB0_1232
	v_cmp_eq_u32_sdwa s[0:1], v23, v36 src0_sel:WORD_1 src1_sel:DWORD
	v_cmp_lt_i32_e32 vcc, v34, v37
	s_and_b64 s[34:35], s[0:1], vcc
	s_mov_b64 s[0:1], 0
	s_and_saveexec_b64 s[30:31], s[34:35]
	v_add_u32_e32 v2, v34, v35
	s_mov_b64 s[0:1], exec
	v_mov_b64_e32 v[20:21], v[2:3]
	s_or_b64 exec, exec, s[30:31]
	s_and_b64 s[0:1], s[0:1], exec
	s_andn2_saveexec_b64 s[24:25], s[24:25]
	s_cbranch_execnz .LBB0_1233

.LBB0_976:
	ds_read_u16 v2, v50 offset:36928
	s_waitcnt lgkmcnt(0)
	v_cmp_ne_u16_e32 vcc, 0, v2
	s_and_saveexec_b64 s[18:19], vcc
	s_cbranch_execz .LBB0_1103
	ds_read_u16 v2, v49 offset:36928
	s_waitcnt vmcnt(5)
	v_add_u32_e32 v20, 0x11240, v49
	ds_read_b32 v20, v20
	v_lshl_add_u64 v[22:23], v[40:41], 0, s[16:17]
	s_mov_b64 s[0:1], 0x200
	s_waitcnt lgkmcnt(1)
	v_lshrrev_b32_e32 v21, 8, v2
	v_and_b32_e32 v2, 0xff, v2
	v_cndmask_b32_e64 v21, v21, 0, s[22:23]
	v_cndmask_b32_e64 v2, v2, 0, s[22:23]
	s_waitcnt vmcnt(4) lgkmcnt(0)
	v_add_u32_sdwa v26, v21, v20 dst_sel:DWORD dst_unused:UNUSED_PAD src0_sel:DWORD src1_sel:WORD_1
	v_add_u32_sdwa v27, v2, v20 dst_sel:DWORD dst_unused:UNUSED_PAD src0_sel:DWORD src1_sel:WORD_0
	v_lshl_add_u64 v[20:21], v[22:23], 0, s[0:1]
	s_waitcnt vmcnt(2)
	v_min_i32_e32 v2, v26, v37
	v_add_u32_e32 v2, v2, v27
	v_sub_u32_e32 v26, v37, v26
	v_med3_i32 v27, v26, 0, 1
	v_sub_u32_e32 v27, v36, v27
	v_cmp_gt_i32_sdwa s[0:1], v16, v27 src0_sel:WORD_0 src1_sel:DWORD
	v_cmp_eq_u32_sdwa s[24:25], v16, v36 src0_sel:WORD_0 src1_sel:DWORD
	v_lshl_add_u64 v[24:25], v[2:3], 1, v[38:39]
	s_and_saveexec_b64 s[28:29], s[0:1]
	global_store_short v[24:25], v20, off
	s_mov_b64 exec, s[28:29]
	v_addc_co_u32_e64 v2, vcc, 0, v2, s[0:1]
	v_subb_co_u32_e64 v26, vcc, v26, 0, s[24:25]
	v_add_u32_e32 v24, 0x201, v22
	v_med3_i32 v27, v26, 0, 1
	v_sub_u32_e32 v27, v36, v27
	v_cmp_gt_i32_sdwa s[0:1], v16, v27 src0_sel:WORD_1 src1_sel:DWORD
	v_cmp_eq_u32_sdwa s[24:25], v16, v36 src0_sel:WORD_1 src1_sel:DWORD
	v_lshl_add_u64 v[28:29], v[2:3], 1, v[38:39]
	s_and_saveexec_b64 s[28:29], s[0:1]
	global_store_short v[28:29], v24, off
	s_mov_b64 exec, s[28:29]
	v_addc_co_u32_e64 v2, vcc, 0, v2, s[0:1]
	v_subb_co_u32_e64 v26, vcc, v26, 0, s[24:25]
	v_add_u32_e32 v24, 0x202, v22
	v_med3_i32 v27, v26, 0, 1
	v_sub_u32_e32 v27, v36, v27
	v_cmp_gt_i32_sdwa s[0:1], v17, v27 src0_sel:WORD_0 src1_sel:DWORD
	v_cmp_eq_u32_sdwa s[24:25], v17, v36 src0_sel:WORD_0 src1_sel:DWORD
	v_lshl_add_u64 v[28:29], v[2:3], 1, v[38:39]
	s_and_saveexec_b64 s[28:29], s[0:1]
	global_store_short v[28:29], v24, off
	s_mov_b64 exec, s[28:29]
	v_addc_co_u32_e64 v2, vcc, 0, v2, s[0:1]
	v_subb_co_u32_e64 v26, vcc, v26, 0, s[24:25]
	v_add_u32_e32 v24, 0x203, v22
	v_med3_i32 v27, v26, 0, 1
	v_sub_u32_e32 v27, v36, v27
	v_cmp_gt_i32_sdwa s[0:1], v17, v27 src0_sel:WORD_1 src1_sel:DWORD
	v_cmp_eq_u32_sdwa s[24:25], v17, v36 src0_sel:WORD_1 src1_sel:DWORD
	v_lshl_add_u64 v[16:17], v[2:3], 1, v[38:39]
	s_and_saveexec_b64 s[28:29], s[0:1]
	global_store_short v[16:17], v24, off
	s_mov_b64 exec, s[28:29]
	v_addc_co_u32_e64 v2, vcc, 0, v2, s[0:1]
	v_subb_co_u32_e64 v26, vcc, v26, 0, s[24:25]
	v_add_u32_e32 v16, 0x204, v22
	v_med3_i32 v27, v26, 0, 1
	v_sub_u32_e32 v27, v36, v27
	v_cmp_gt_i32_sdwa s[0:1], v18, v27 src0_sel:WORD_0 src1_sel:DWORD
	v_cmp_eq_u32_sdwa s[24:25], v18, v36 src0_sel:WORD_0 src1_sel:DWORD
	v_lshl_add_u64 v[24:25], v[2:3], 1, v[38:39]
	s_and_saveexec_b64 s[28:29], s[0:1]
	global_store_short v[24:25], v16, off
	s_mov_b64 exec, s[28:29]
	v_addc_co_u32_e64 v2, vcc, 0, v2, s[0:1]
	v_subb_co_u32_e64 v26, vcc, v26, 0, s[24:25]
	v_add_u32_e32 v16, 0x205, v22
	v_med3_i32 v27, v26, 0, 1
	v_sub_u32_e32 v27, v36, v27
	v_cmp_gt_i32_sdwa s[0:1], v18, v27 src0_sel:WORD_1 src1_sel:DWORD
	v_cmp_eq_u32_sdwa s[24:25], v18, v36 src0_sel:WORD_1 src1_sel:DWORD
	v_lshl_add_u64 v[24:25], v[2:3], 1, v[38:39]
	s_and_saveexec_b64 s[28:29], s[0:1]
	global_store_short v[24:25], v16, off
	s_mov_b64 exec, s[28:29]
	v_addc_co_u32_e64 v2, vcc, 0, v2, s[0:1]
	v_subb_co_u32_e64 v26, vcc, v26, 0, s[24:25]
	v_add_u32_e32 v16, 0x206, v22
	v_med3_i32 v27, v26, 0, 1
	v_sub_u32_e32 v27, v36, v27
	v_cmp_gt_i32_sdwa s[0:1], v19, v27 src0_sel:WORD_0 src1_sel:DWORD
	v_cmp_eq_u32_sdwa s[24:25], v19, v36 src0_sel:WORD_0 src1_sel:DWORD
	v_lshl_add_u64 v[24:25], v[2:3], 1, v[38:39]
	s_and_saveexec_b64 s[28:29], s[0:1]
	global_store_short v[24:25], v16, off
	s_mov_b64 exec, s[28:29]
	v_addc_co_u32_e64 v2, vcc, 0, v2, s[0:1]
	v_subb_co_u32_e64 v26, vcc, v26, 0, s[24:25]
	v_add_u32_e32 v16, 0x207, v22
	v_med3_i32 v27, v26, 0, 1
	v_sub_u32_e32 v27, v36, v27
	v_cmp_gt_i32_sdwa s[0:1], v19, v27 src0_sel:WORD_1 src1_sel:DWORD
	v_cmp_eq_u32_sdwa s[24:25], v19, v36 src0_sel:WORD_1 src1_sel:DWORD
	v_lshl_add_u64 v[18:19], v[2:3], 1, v[38:39]
	s_and_saveexec_b64 s[28:29], s[0:1]
	global_store_short v[18:19], v16, off
	s_mov_b64 exec, s[28:29]
	v_addc_co_u32_e64 v2, vcc, 0, v2, s[0:1]
	v_subb_co_u32_e64 v26, vcc, v26, 0, s[24:25]
	v_add_u32_e32 v16, 0x208, v22
	v_med3_i32 v27, v26, 0, 1
	v_sub_u32_e32 v27, v36, v27
	v_cmp_gt_i32_sdwa s[0:1], v12, v27 src0_sel:WORD_0 src1_sel:DWORD
	v_cmp_eq_u32_sdwa s[24:25], v12, v36 src0_sel:WORD_0 src1_sel:DWORD
	v_lshl_add_u64 v[18:19], v[2:3], 1, v[38:39]
	s_and_saveexec_b64 s[28:29], s[0:1]
	global_store_short v[18:19], v16, off
	s_mov_b64 exec, s[28:29]
	v_addc_co_u32_e64 v2, vcc, 0, v2, s[0:1]
	v_subb_co_u32_e64 v26, vcc, v26, 0, s[24:25]
	v_add_u32_e32 v16, 0x209, v22
	v_med3_i32 v27, v26, 0, 1
	v_sub_u32_e32 v27, v36, v27
	v_cmp_gt_i32_sdwa s[0:1], v12, v27 src0_sel:WORD_1 src1_sel:DWORD
	v_cmp_eq_u32_sdwa s[24:25], v12, v36 src0_sel:WORD_1 src1_sel:DWORD
	v_lshl_add_u64 v[18:19], v[2:3], 1, v[38:39]
	s_and_saveexec_b64 s[28:29], s[0:1]
	global_store_short v[18:19], v16, off
	s_mov_b64 exec, s[28:29]
	v_addc_co_u32_e64 v2, vcc, 0, v2, s[0:1]
	v_subb_co_u32_e64 v26, vcc, v26, 0, s[24:25]
	v_add_u32_e32 v16, 0x20a, v22
	v_med3_i32 v27, v26, 0, 1
	v_sub_u32_e32 v27, v36, v27
	v_cmp_gt_i32_sdwa s[0:1], v13, v27 src0_sel:WORD_0 src1_sel:DWORD
	v_cmp_eq_u32_sdwa s[24:25], v13, v36 src0_sel:WORD_0 src1_sel:DWORD
	v_lshl_add_u64 v[18:19], v[2:3], 1, v[38:39]
	s_and_saveexec_b64 s[28:29], s[0:1]
	global_store_short v[18:19], v16, off
	s_mov_b64 exec, s[28:29]
	v_addc_co_u32_e64 v2, vcc, 0, v2, s[0:1]
	v_subb_co_u32_e64 v26, vcc, v26, 0, s[24:25]
	v_add_u32_e32 v16, 0x20b, v22
	v_med3_i32 v27, v26, 0, 1
	v_sub_u32_e32 v27, v36, v27
	v_cmp_gt_i32_sdwa s[0:1], v13, v27 src0_sel:WORD_1 src1_sel:DWORD
	v_cmp_eq_u32_sdwa s[24:25], v13, v36 src0_sel:WORD_1 src1_sel:DWORD
	v_lshl_add_u64 v[12:13], v[2:3], 1, v[38:39]
	s_and_saveexec_b64 s[28:29], s[0:1]
	global_store_short v[12:13], v16, off
	s_mov_b64 exec, s[28:29]
	v_addc_co_u32_e64 v2, vcc, 0, v2, s[0:1]
	v_subb_co_u32_e64 v26, vcc, v26, 0, s[24:25]
	v_add_u32_e32 v12, 0x20c, v22
	v_med3_i32 v27, v26, 0, 1
	v_sub_u32_e32 v27, v36, v27
	v_cmp_gt_i32_sdwa s[0:1], v14, v27 src0_sel:WORD_0 src1_sel:DWORD
	v_cmp_eq_u32_sdwa s[24:25], v14, v36 src0_sel:WORD_0 src1_sel:DWORD
	v_lshl_add_u64 v[16:17], v[2:3], 1, v[38:39]
	s_and_saveexec_b64 s[28:29], s[0:1]
	global_store_short v[16:17], v12, off
	s_mov_b64 exec, s[28:29]
	v_addc_co_u32_e64 v2, vcc, 0, v2, s[0:1]
	v_subb_co_u32_e64 v26, vcc, v26, 0, s[24:25]
	v_add_u32_e32 v12, 0x20d, v22
	v_med3_i32 v27, v26, 0, 1
	v_sub_u32_e32 v27, v36, v27
	v_cmp_gt_i32_sdwa s[0:1], v14, v27 src0_sel:WORD_1 src1_sel:DWORD
	v_cmp_eq_u32_sdwa s[24:25], v14, v36 src0_sel:WORD_1 src1_sel:DWORD
	v_lshl_add_u64 v[16:17], v[2:3], 1, v[38:39]
	s_and_saveexec_b64 s[28:29], s[0:1]
	global_store_short v[16:17], v12, off
	s_mov_b64 exec, s[28:29]
	v_addc_co_u32_e64 v2, vcc, 0, v2, s[0:1]
	v_subb_co_u32_e64 v26, vcc, v26, 0, s[24:25]
	v_add_u32_e32 v12, 0x20e, v22
	v_med3_i32 v27, v26, 0, 1
	v_sub_u32_e32 v27, v36, v27
	v_cmp_gt_i32_sdwa s[0:1], v15, v27 src0_sel:WORD_0 src1_sel:DWORD
	v_cmp_eq_u32_sdwa s[24:25], v15, v36 src0_sel:WORD_0 src1_sel:DWORD
	v_lshl_add_u64 v[16:17], v[2:3], 1, v[38:39]
	s_and_saveexec_b64 s[28:29], s[0:1]
	global_store_short v[16:17], v12, off
	s_mov_b64 exec, s[28:29]
	v_addc_co_u32_e64 v2, vcc, 0, v2, s[0:1]
	v_subb_co_u32_e64 v26, vcc, v26, 0, s[24:25]
	v_sub_u32_e32 v26, v37, v26
	v_min_i32_e32 v27, v26, v37
	v_sub_u32_e32 v27, v2, v27
	v_cmp_le_u32_sdwa s[24:25], v15, v36 src0_sel:WORD_1 src1_sel:DWORD
	s_mov_b64 s[0:1], 0
	s_and_saveexec_b64 s[28:29], s[24:25]
	s_xor_b64 s[24:25], exec, s[28:29]
	s_cbranch_execz .LBB0_1234
	v_cmp_eq_u32_sdwa s[0:1], v15, v36 src0_sel:WORD_1 src1_sel:DWORD
	v_cmp_lt_i32_e32 vcc, v26, v37
	s_and_b64 s[30:31], s[0:1], vcc
	s_mov_b64 s[0:1], 0
	s_and_saveexec_b64 s[28:29], s[30:31]
	v_add_u32_e32 v2, v26, v27
	s_mov_b64 s[0:1], exec
	v_mov_b64_e32 v[12:13], v[2:3]
	s_or_b64 exec, exec, s[28:29]
	s_and_b64 s[0:1], s[0:1], exec
	s_andn2_saveexec_b64 s[24:25], s[24:25]
	s_cbranch_execnz .LBB0_1235

.LBB0_1104:
	ds_read_u16 v2, v50 offset:36960
	s_waitcnt lgkmcnt(0)
	v_cmp_ne_u16_e32 vcc, 0, v2
	s_and_saveexec_b64 s[18:19], vcc
	s_cbranch_execz .LBB0_710
	ds_read_u16 v2, v49 offset:36960
	s_waitcnt vmcnt(3)
	v_add_u32_e32 v12, 0x11260, v49
	ds_read_b32 v12, v12
	v_lshl_add_u64 v[14:15], v[40:41], 0, s[16:17]
	s_mov_b64 s[0:1], 0x300
	s_waitcnt lgkmcnt(1)
	v_lshrrev_b32_e32 v13, 8, v2
	v_and_b32_e32 v2, 0xff, v2
	v_cndmask_b32_e64 v13, v13, 0, s[22:23]
	v_cndmask_b32_e64 v2, v2, 0, s[22:23]
	s_waitcnt vmcnt(2) lgkmcnt(0)
	v_add_u32_sdwa v18, v13, v12 dst_sel:DWORD dst_unused:UNUSED_PAD src0_sel:DWORD src1_sel:WORD_1
	v_add_u32_sdwa v19, v2, v12 dst_sel:DWORD dst_unused:UNUSED_PAD src0_sel:DWORD src1_sel:WORD_0
	v_lshl_add_u64 v[12:13], v[14:15], 0, s[0:1]
	s_waitcnt vmcnt(0)
	v_min_i32_e32 v2, v18, v37
	v_add_u32_e32 v2, v2, v19
	v_sub_u32_e32 v18, v37, v18
	v_med3_i32 v19, v18, 0, 1
	v_sub_u32_e32 v19, v36, v19
	v_cmp_gt_i32_sdwa s[0:1], v8, v19 src0_sel:WORD_0 src1_sel:DWORD
	v_cmp_eq_u32_sdwa s[24:25], v8, v36 src0_sel:WORD_0 src1_sel:DWORD
	v_lshl_add_u64 v[16:17], v[2:3], 1, v[38:39]
	s_and_saveexec_b64 s[26:27], s[0:1]
	global_store_short v[16:17], v12, off
	s_mov_b64 exec, s[26:27]
	v_addc_co_u32_e64 v2, vcc, 0, v2, s[0:1]
	v_subb_co_u32_e64 v18, vcc, v18, 0, s[24:25]
	v_add_u32_e32 v16, 0x301, v14
	v_med3_i32 v19, v18, 0, 1
	v_sub_u32_e32 v19, v36, v19
	v_cmp_gt_i32_sdwa s[0:1], v8, v19 src0_sel:WORD_1 src1_sel:DWORD
	v_cmp_eq_u32_sdwa s[24:25], v8, v36 src0_sel:WORD_1 src1_sel:DWORD
	v_lshl_add_u64 v[20:21], v[2:3], 1, v[38:39]
	s_and_saveexec_b64 s[26:27], s[0:1]
	global_store_short v[20:21], v16, off
	s_mov_b64 exec, s[26:27]
	v_addc_co_u32_e64 v2, vcc, 0, v2, s[0:1]
	v_subb_co_u32_e64 v18, vcc, v18, 0, s[24:25]
	v_add_u32_e32 v16, 0x302, v14
	v_med3_i32 v19, v18, 0, 1
	v_sub_u32_e32 v19, v36, v19
	v_cmp_gt_i32_sdwa s[0:1], v9, v19 src0_sel:WORD_0 src1_sel:DWORD
	v_cmp_eq_u32_sdwa s[24:25], v9, v36 src0_sel:WORD_0 src1_sel:DWORD
	v_lshl_add_u64 v[20:21], v[2:3], 1, v[38:39]
	s_and_saveexec_b64 s[26:27], s[0:1]
	global_store_short v[20:21], v16, off
	s_mov_b64 exec, s[26:27]
	v_addc_co_u32_e64 v2, vcc, 0, v2, s[0:1]
	v_subb_co_u32_e64 v18, vcc, v18, 0, s[24:25]
	v_add_u32_e32 v16, 0x303, v14
	v_med3_i32 v19, v18, 0, 1
	v_sub_u32_e32 v19, v36, v19
	v_cmp_gt_i32_sdwa s[0:1], v9, v19 src0_sel:WORD_1 src1_sel:DWORD
	v_cmp_eq_u32_sdwa s[24:25], v9, v36 src0_sel:WORD_1 src1_sel:DWORD
	v_lshl_add_u64 v[8:9], v[2:3], 1, v[38:39]
	s_and_saveexec_b64 s[26:27], s[0:1]
	global_store_short v[8:9], v16, off
	s_mov_b64 exec, s[26:27]
	v_addc_co_u32_e64 v2, vcc, 0, v2, s[0:1]
	v_subb_co_u32_e64 v18, vcc, v18, 0, s[24:25]
	v_add_u32_e32 v8, 0x304, v14
	v_med3_i32 v19, v18, 0, 1
	v_sub_u32_e32 v19, v36, v19
	v_cmp_gt_i32_sdwa s[0:1], v10, v19 src0_sel:WORD_0 src1_sel:DWORD
	v_cmp_eq_u32_sdwa s[24:25], v10, v36 src0_sel:WORD_0 src1_sel:DWORD
	v_lshl_add_u64 v[16:17], v[2:3], 1, v[38:39]
	s_and_saveexec_b64 s[26:27], s[0:1]
	global_store_short v[16:17], v8, off
	s_mov_b64 exec, s[26:27]
	v_addc_co_u32_e64 v2, vcc, 0, v2, s[0:1]
	v_subb_co_u32_e64 v18, vcc, v18, 0, s[24:25]
	v_add_u32_e32 v8, 0x305, v14
	v_med3_i32 v19, v18, 0, 1
	v_sub_u32_e32 v19, v36, v19
	v_cmp_gt_i32_sdwa s[0:1], v10, v19 src0_sel:WORD_1 src1_sel:DWORD
	v_cmp_eq_u32_sdwa s[24:25], v10, v36 src0_sel:WORD_1 src1_sel:DWORD
	v_lshl_add_u64 v[16:17], v[2:3], 1, v[38:39]
	s_and_saveexec_b64 s[26:27], s[0:1]
	global_store_short v[16:17], v8, off
	s_mov_b64 exec, s[26:27]
	v_addc_co_u32_e64 v2, vcc, 0, v2, s[0:1]
	v_subb_co_u32_e64 v18, vcc, v18, 0, s[24:25]
	v_add_u32_e32 v8, 0x306, v14
	v_med3_i32 v19, v18, 0, 1
	v_sub_u32_e32 v19, v36, v19
	v_cmp_gt_i32_sdwa s[0:1], v11, v19 src0_sel:WORD_0 src1_sel:DWORD
	v_cmp_eq_u32_sdwa s[24:25], v11, v36 src0_sel:WORD_0 src1_sel:DWORD
	v_lshl_add_u64 v[16:17], v[2:3], 1, v[38:39]
	s_and_saveexec_b64 s[26:27], s[0:1]
	global_store_short v[16:17], v8, off
	s_mov_b64 exec, s[26:27]
	v_addc_co_u32_e64 v2, vcc, 0, v2, s[0:1]
	v_subb_co_u32_e64 v18, vcc, v18, 0, s[24:25]
	v_add_u32_e32 v8, 0x307, v14
	v_med3_i32 v19, v18, 0, 1
	v_sub_u32_e32 v19, v36, v19
	v_cmp_gt_i32_sdwa s[0:1], v11, v19 src0_sel:WORD_1 src1_sel:DWORD
	v_cmp_eq_u32_sdwa s[24:25], v11, v36 src0_sel:WORD_1 src1_sel:DWORD
	v_lshl_add_u64 v[10:11], v[2:3], 1, v[38:39]
	s_and_saveexec_b64 s[26:27], s[0:1]
	global_store_short v[10:11], v8, off
	s_mov_b64 exec, s[26:27]
	v_addc_co_u32_e64 v2, vcc, 0, v2, s[0:1]
	v_subb_co_u32_e64 v18, vcc, v18, 0, s[24:25]
	v_add_u32_e32 v8, 0x308, v14
	v_med3_i32 v19, v18, 0, 1
	v_sub_u32_e32 v19, v36, v19
	v_cmp_gt_i32_sdwa s[0:1], v4, v19 src0_sel:WORD_0 src1_sel:DWORD
	v_cmp_eq_u32_sdwa s[24:25], v4, v36 src0_sel:WORD_0 src1_sel:DWORD
	v_lshl_add_u64 v[10:11], v[2:3], 1, v[38:39]
	s_and_saveexec_b64 s[26:27], s[0:1]
	global_store_short v[10:11], v8, off
	s_mov_b64 exec, s[26:27]
	v_addc_co_u32_e64 v2, vcc, 0, v2, s[0:1]
	v_subb_co_u32_e64 v18, vcc, v18, 0, s[24:25]
	v_add_u32_e32 v8, 0x309, v14
	v_med3_i32 v19, v18, 0, 1
	v_sub_u32_e32 v19, v36, v19
	v_cmp_gt_i32_sdwa s[0:1], v4, v19 src0_sel:WORD_1 src1_sel:DWORD
	v_cmp_eq_u32_sdwa s[24:25], v4, v36 src0_sel:WORD_1 src1_sel:DWORD
	v_lshl_add_u64 v[10:11], v[2:3], 1, v[38:39]
	s_and_saveexec_b64 s[26:27], s[0:1]
	global_store_short v[10:11], v8, off
	s_mov_b64 exec, s[26:27]
	v_addc_co_u32_e64 v2, vcc, 0, v2, s[0:1]
	v_subb_co_u32_e64 v18, vcc, v18, 0, s[24:25]
	v_add_u32_e32 v8, 0x30a, v14
	v_med3_i32 v19, v18, 0, 1
	v_sub_u32_e32 v19, v36, v19
	v_cmp_gt_i32_sdwa s[0:1], v5, v19 src0_sel:WORD_0 src1_sel:DWORD
	v_cmp_eq_u32_sdwa s[24:25], v5, v36 src0_sel:WORD_0 src1_sel:DWORD
	v_lshl_add_u64 v[10:11], v[2:3], 1, v[38:39]
	s_and_saveexec_b64 s[26:27], s[0:1]
	global_store_short v[10:11], v8, off
	s_mov_b64 exec, s[26:27]
	v_addc_co_u32_e64 v2, vcc, 0, v2, s[0:1]
	v_subb_co_u32_e64 v18, vcc, v18, 0, s[24:25]
	v_add_u32_e32 v8, 0x30b, v14
	v_med3_i32 v19, v18, 0, 1
	v_sub_u32_e32 v19, v36, v19
	v_cmp_gt_i32_sdwa s[0:1], v5, v19 src0_sel:WORD_1 src1_sel:DWORD
	v_cmp_eq_u32_sdwa s[24:25], v5, v36 src0_sel:WORD_1 src1_sel:DWORD
	v_lshl_add_u64 v[4:5], v[2:3], 1, v[38:39]
	s_and_saveexec_b64 s[26:27], s[0:1]
	global_store_short v[4:5], v8, off
	s_mov_b64 exec, s[26:27]
	v_addc_co_u32_e64 v2, vcc, 0, v2, s[0:1]
	v_subb_co_u32_e64 v18, vcc, v18, 0, s[24:25]
	v_add_u32_e32 v4, 0x30c, v14
	v_med3_i32 v19, v18, 0, 1
	v_sub_u32_e32 v19, v36, v19
	v_cmp_gt_i32_sdwa s[0:1], v6, v19 src0_sel:WORD_0 src1_sel:DWORD
	v_cmp_eq_u32_sdwa s[24:25], v6, v36 src0_sel:WORD_0 src1_sel:DWORD
	v_lshl_add_u64 v[8:9], v[2:3], 1, v[38:39]
	s_and_saveexec_b64 s[26:27], s[0:1]
	global_store_short v[8:9], v4, off
	s_mov_b64 exec, s[26:27]
	v_addc_co_u32_e64 v2, vcc, 0, v2, s[0:1]
	v_subb_co_u32_e64 v18, vcc, v18, 0, s[24:25]
	v_add_u32_e32 v4, 0x30d, v14
	v_med3_i32 v19, v18, 0, 1
	v_sub_u32_e32 v19, v36, v19
	v_cmp_gt_i32_sdwa s[0:1], v6, v19 src0_sel:WORD_1 src1_sel:DWORD
	v_cmp_eq_u32_sdwa s[24:25], v6, v36 src0_sel:WORD_1 src1_sel:DWORD
	v_lshl_add_u64 v[8:9], v[2:3], 1, v[38:39]
	s_and_saveexec_b64 s[26:27], s[0:1]
	global_store_short v[8:9], v4, off
	s_mov_b64 exec, s[26:27]
	v_addc_co_u32_e64 v2, vcc, 0, v2, s[0:1]
	v_subb_co_u32_e64 v18, vcc, v18, 0, s[24:25]
	v_add_u32_e32 v4, 0x30e, v14
	v_med3_i32 v19, v18, 0, 1
	v_sub_u32_e32 v19, v36, v19
	v_cmp_gt_i32_sdwa s[0:1], v7, v19 src0_sel:WORD_0 src1_sel:DWORD
	v_cmp_eq_u32_sdwa s[24:25], v7, v36 src0_sel:WORD_0 src1_sel:DWORD
	v_lshl_add_u64 v[8:9], v[2:3], 1, v[38:39]
	s_and_saveexec_b64 s[26:27], s[0:1]
	global_store_short v[8:9], v4, off
	s_mov_b64 exec, s[26:27]
	v_addc_co_u32_e64 v2, vcc, 0, v2, s[0:1]
	v_subb_co_u32_e64 v18, vcc, v18, 0, s[24:25]
	v_sub_u32_e32 v18, v37, v18
	v_min_i32_e32 v19, v18, v37
	v_sub_u32_e32 v19, v2, v19
	v_cmp_le_u32_sdwa s[24:25], v7, v36 src0_sel:WORD_1 src1_sel:DWORD
	s_mov_b64 s[0:1], 0
	s_and_saveexec_b64 s[26:27], s[24:25]
	s_xor_b64 s[24:25], exec, s[26:27]
	s_cbranch_execz .LBB0_1236
	v_cmp_eq_u32_sdwa s[0:1], v7, v36 src0_sel:WORD_1 src1_sel:DWORD
	v_cmp_lt_i32_e32 vcc, v18, v37
	s_and_b64 s[28:29], s[0:1], vcc
	s_mov_b64 s[0:1], 0
	s_and_saveexec_b64 s[26:27], s[28:29]
	v_add_u32_e32 v2, v18, v19
	s_mov_b64 s[0:1], exec
	v_mov_b64_e32 v[4:5], v[2:3]
	s_or_b64 exec, exec, s[26:27]
	s_and_b64 s[0:1], s[0:1], exec
	s_andn2_saveexec_b64 s[24:25], s[24:25]
	s_cbranch_execnz .LBB0_1237
